# baseline (speedup 1.0000x reference)
_Z8k5_finalPK15HIP_vector_typeIjLj2EEPKfS4_PyPf:
	s_load_dwordx2 s[4:5], s[0:1], 0x0
	s_load_dwordx4 s[8:11], s[0:1], 0x18
	s_load_dwordx4 s[12:15], s[0:1], 0x8
	s_ashr_i32 s3, s2, 31
	s_lshl_b64 s[6:7], s[2:3], 15
	v_lshlrev_b32_e32 v1, 5, v0
	s_waitcnt lgkmcnt(0)
	s_add_u32 s4, s4, s6
	s_addc_u32 s5, s5, s7
	global_load_dwordx4 v[6:9], v1, s[4:5] offset:16
	global_load_dwordx4 v[2:5], v1, s[4:5]
	s_cmp_eq_u32 s2, 0
	s_cselect_b64 s[6:7], -1, 0
	s_cmp_lg_u32 s2, 0
	v_mov_b32_e32 v1, 0
	s_cbranch_scc1 .LBB4_6
	s_movk_i32 s2, 0x100
	v_cmp_gt_u32_e32 vcc, s2, v0
	v_mov_b32_e32 v1, 0
	s_and_saveexec_b64 s[2:3], vcc
	s_cbranch_execz .LBB4_3
	v_lshlrev_b32_e32 v1, 2, v0
	global_load_dword v1, v1, s[14:15]
.LBB4_3:
	s_or_b64 exec, exec, s[2:3]
	s_and_saveexec_b64 s[2:3], vcc
	s_cbranch_execz .LBB4_5
	v_mul_u32_u24_e32 v10, 12, v0
	v_lshlrev_b32_e32 v22, 2, v10
	global_load_dwordx4 v[10:13], v22, s[12:13]
	global_load_dwordx4 v[14:17], v22, s[12:13] offset:16
	global_load_dwordx4 v[18:21], v22, s[12:13] offset:32
	s_waitcnt vmcnt(2)
	ds_write_b128 v22, v[10:13]
	s_waitcnt vmcnt(1)
	ds_write_b128 v22, v[14:17] offset:16
	s_waitcnt vmcnt(0)
	ds_write_b128 v22, v[18:21] offset:32
